# attention loop back edge rotated: loop-carried updates, exit test and end-of-iteration wait selector all placed before the loop-back barrier (one branch after it instead of twelve instructions)
# speedup vs baseline: 1.0075x; 1.0017x over previous
.LBB0_1344:
	s_waitcnt lgkmcnt(6)
	v_mfma_f32_32x32x16_bf16 v[2:17], v[82:85], v[90:93], v[2:17]
	v_exp_f32_e32 v34, v34
	v_exp_f32_e32 v35, v35
	v_exp_f32_e32 v36, v36
	v_exp_f32_e32 v37, v37
	s_waitcnt lgkmcnt(4)
	v_mfma_f32_32x32x16_bf16 v[18:33], v[82:85], v[86:89], v[18:33]
	v_exp_f32_e32 v38, v38
	v_exp_f32_e32 v39, v39
	v_exp_f32_e32 v40, v40
	v_exp_f32_e32 v41, v41
	s_waitcnt lgkmcnt(2)
	v_mfma_f32_32x32x16_bf16 v[2:17], v[66:69], v[70:73], v[2:17]
	v_exp_f32_e32 v42, v42
	v_exp_f32_e32 v43, v43
	v_exp_f32_e32 v44, v44
	v_exp_f32_e32 v45, v45
	s_waitcnt lgkmcnt(0)
	v_mfma_f32_32x32x16_bf16 v[18:33], v[66:69], v[74:77], v[18:33]
	v_exp_f32_e32 v46, v46
	v_exp_f32_e32 v47, v47
	v_exp_f32_e32 v48, v48
	v_exp_f32_e32 v49, v49
	s_and_b64 s[44:45], s[52:53], exec
	s_cselect_b32 s58, s69, 0
	s_add_i32 s58, s58, s101
	v_add_f32_e32 v66, v193, v166
	v_add_f32_e32 v193, v66, v94
	v_add_u32_e32 v195, 0x80, v195
	v_lshl_add_u64 v[218:219], v[218:219], 0, s[82:83]
	v_lshl_add_u64 v[220:221], v[220:221], 0, s[96:97]
	v_lshl_add_u64 v[222:223], v[222:223], 0, s[82:83]
	s_mov_b32 s44, s61
	s_and_b64 vcc, exec, s[50:51]
	s_cmp_eq_u32 s58, 3
	s_cbranch_scc1 .Lattn_w3b
	s_cmp_eq_u32 s58, 2
	s_cbranch_scc1 .Lattn_w2b
	s_cmp_eq_u32 s58, 1
	s_cbranch_scc1 .Lattn_w1b
	s_waitcnt vmcnt(0) lgkmcnt(0)
	s_barrier
	s_branch .Lattn_tail
.Lattn_w1b:
	s_waitcnt vmcnt(1) lgkmcnt(0)
	s_barrier
	s_branch .Lattn_tail

.Lattn_tail:
	s_cbranch_vccz .LBB0_1319
